# converters at the NA tail / out-proj L1 end stop when 60 of 64 GLA workgroups / 248 of 256 workgroups are done (wind-down overlaps the last arrivals)
# baseline (speedup 1.0000x reference)
; #define LAS __attribute__((address_space(3)))
; __device__ __forceinline__ void lds_barrier() { asm volatile("s_waitcnt lgkmcnt(0)" ::: "memory"); __builtin_amdgcn_s_barrier(); asm volatile("" ::: "memory"); }
; __device__ __forceinline__ unsigned xb_add(unsigned* p, unsigned v) { return __hip_atomic_fetch_add(p, v, __ATOMIC_RELAXED, __HIP_MEMORY_SCOPE_AGENT); }
; __device__ __forceinline__ void phase_prologue(const Args& a, LAS unsigned char* lds) {
;     ...
;     unsigned* cq_head = (unsigned*)(a.ws + WS_CTL) + 8192 + 768;
;     volatile LAS int* qs = (volatile LAS int*)(lds + 128 * 129 * 4);
;     int pend = 0, it = 0;
;     if (tid == 0) { qs[0] = (int)xb_add(cq_head, 1u); pend = (int)xb_add(cq_head, 1u); }
;     __syncthreads();
;     for (int u = qs[0]; u < CTOT; u = qs[it & 1]) {
;     ...
;         const int kt = r / NT, ntl = r % NT, k0 = kt * 128, n0 = ntl * 128;
;         const int drow0 = mode == 0 ? n0 : (ntl * 256 + (mode == 2 ? 128 : 0));
;         f32x4 v[8];
; #pragma unroll
;         for (int i = 0; i < 8; ++i) { const int id = tid + 512 * i, row = id >> 5, c4 = id & 31, n = n0 + c4 * 4;
;             v[i] = (f32x4){0.f, 0.f, 0.f, 0.f};
;             if (n < nvalid) v[i] = *(const f32x4*)(src + (size_t)(k0 + row) * ldn + n); }
; #pragma unroll
;         for (int i = 0; i < 8; ++i) { const int id = tid + 512 * i, row = id >> 5, c4 = id & 31;
;             LAS float* tp = tile + row * 129 + c4 * 4; tp[0] = v[i][0]; tp[1] = v[i][1]; tp[2] = v[i][2]; tp[3] = v[i][3]; }
;         lds_barrier();
; #pragma unroll
;         for (int i = 0; i < 4; ++i) { const int piece = tid + 512 * i, nl = piece >> 4, kg = piece & 15; const LAS float* s = tile + (kg * 8) * 129 + nl;
;             u32x4 o; o.x = pk2(s[0], s[129]); o.y = pk2(s[258], s[387]); o.z = pk2(s[516], s[645]); o.w = pk2(s[774], s[903]);
;             *(u32x4*)(dst + (size_t)(drow0 + nl) * 2048 + k0 + kg * 8) = o; }
.Lcva_f0:
	s_mov_b64 exec, s[34:35]
	s_waitcnt lgkmcnt(0)
	s_barrier
	ds_read_b32 v127, v125 offset:4
	s_waitcnt lgkmcnt(0)
	v_readfirstlane_b32 s25, v127
	s_cmpk_ge_u32 s25, 0x3c
	s_cbranch_scc1 .Lcva_done
	s_barrier
	v_lshrrev_b32_e32 v104, 5, v0
	v_and_b32_e32 v126, 31, v0
	v_lshlrev_b32_e32 v105, 13, v104
	v_lshl_add_u32 v105, v126, 4, v105
	v_add_u32_e32 v106, 0x20000, v105
	v_add_u32_e32 v107, 0x40000, v105
	v_add_u32_e32 v108, 0x60000, v105
	v_add_u32_e32 v109, 0x80000, v105
	v_add_u32_e32 v110, 0xa0000, v105
	v_add_u32_e32 v111, 0xc0000, v105
	v_add_u32_e32 v112, 0xe0000, v105
	v_mul_u32_u24_e32 v113, 0x204, v104
	v_lshl_add_u32 v113, v126, 4, v113
	v_lshrrev_b32_e32 v127, 4, v0
	v_and_b32_e32 v126, 15, v0
	v_mul_u32_u24_e32 v114, 0x1020, v126
	v_lshl_add_u32 v114, v127, 2, v114
	v_lshlrev_b32_e32 v115, 12, v127
	v_lshl_add_u32 v115, v126, 4, v115
	v_add_u32_e32 v116, 0x20000, v115
	v_add_u32_e32 v117, 0x40000, v115
	v_add_u32_e32 v118, 0x60000, v115
	v_readlane_b32 s42, v254, 27
	v_readlane_b32 s43, v254, 28
	s_sub_u32 s42, s42, 0x28
	s_subb_u32 s43, s43, 0
	s_load_dwordx2 s[40:41], s[42:43], 0x0
	s_waitcnt lgkmcnt(0)
	v_cmp_eq_u32_e32 vcc, 0, v0
	s_and_saveexec_b64 s[34:35], vcc
	s_cbranch_execz .Lcva_t0a
	global_atomic_add v123, v120, v119, s[94:95] sc0
	s_waitcnt vmcnt(0)
	ds_write_b32 v125, v123
	ds_write_b32 v125, v122 offset:4

; __device__ __forceinline__ void lds_barrier() { asm volatile("s_waitcnt lgkmcnt(0)" ::: "memory"); __builtin_amdgcn_s_barrier(); asm volatile("" ::: "memory"); }
; __device__ __forceinline__ unsigned xb_add(unsigned* p, unsigned v) { return __hip_atomic_fetch_add(p, v, __ATOMIC_RELAXED, __HIP_MEMORY_SCOPE_AGENT); }
; __device__ __forceinline__ void phase_prologue(const Args& a, LAS unsigned char* lds) {
;     ...
;     for (int u = qs[0]; u < CTOT; u = qs[it & 1]) {
;         int r = u; const float* src; int ldn, nvalid, NT, mode = 0; bf16_t* dst;
;     ...
;         ++it;
;         if (tid == 0) { qs[it & 1] = pend; pend = (int)xb_add(cq_head, 1u); }
;         lds_barrier();
.Lcva_loop:
	ds_read_b32 v126, v125
	ds_read_b32 v127, v125 offset:4
	s_waitcnt lgkmcnt(0)
	v_readfirstlane_b32 s24, v126
	v_readfirstlane_b32 s25, v127
	s_cmpk_gt_u32 s24, 0x1fff
	s_cbranch_scc1 .Lcva_done
	s_cmpk_ge_u32 s25, 0x3c
	s_cbranch_scc1 .Lcva_nopf
	v_cmp_eq_u32_e32 vcc, 0, v0
	s_and_saveexec_b64 s[34:35], vcc
	s_cbranch_execz .Lcva_t0b
	global_atomic_add v123, v120, v119, s[94:95] sc0
	global_atomic_add v124, v121, v122, s[94:95] sc0

; #define LAS __attribute__((address_space(3)))
; __device__ __forceinline__ void lds_barrier() { asm volatile("s_waitcnt lgkmcnt(0)" ::: "memory"); __builtin_amdgcn_s_barrier(); asm volatile("" ::: "memory"); }
; __device__ __forceinline__ void phase_prologue(const Args& a, LAS unsigned char* lds) {
;     ...
;         else { r -= CJ3; const int which = r / CJM; r -= which * CJM; const int mtx = r >> 8; r &= 255; ldn = 2048; nvalid = 2048; NT = 16;
;             if (which == 0) { src = a.in[I_WGATE] + (size_t)mtx * 2048 * 2048; dst = (bf16_t*)(a.ws + WS_WGU) + (size_t)mtx * 4096 * 2048; mode = 1; }
;             else if (which == 1) { src = a.in[I_WUP] + (size_t)mtx * 2048 * 2048; dst = (bf16_t*)(a.ws + WS_WGU) + (size_t)mtx * 4096 * 2048; mode = 2; }
;             else { src = a.in[I_WDOWN] + (size_t)mtx * 2048 * 2048; dst = (bf16_t*)(a.ws + WS_WDN) + (size_t)mtx * 2048 * 2048; } }
;         const int kt = r / NT, ntl = r % NT, k0 = kt * 128, n0 = ntl * 128;
;         const int drow0 = mode == 0 ? n0 : (ntl * 256 + (mode == 2 ? 128 : 0));
;         f32x4 v[8];
; #pragma unroll
;         for (int i = 0; i < 8; ++i) { const int id = tid + 512 * i, row = id >> 5, c4 = id & 31, n = n0 + c4 * 4;
;             v[i] = (f32x4){0.f, 0.f, 0.f, 0.f};
;             if (n < nvalid) v[i] = *(const f32x4*)(src + (size_t)(k0 + row) * ldn + n); }
; #pragma unroll
;         for (int i = 0; i < 8; ++i) { const int id = tid + 512 * i, row = id >> 5, c4 = id & 31;
;             LAS float* tp = tile + row * 129 + c4 * 4; tp[0] = v[i][0]; tp[1] = v[i][1]; tp[2] = v[i][2]; tp[3] = v[i][3]; }
;         lds_barrier();
; #pragma unroll
;         for (int i = 0; i < 4; ++i) { const int piece = tid + 512 * i, nl = piece >> 4, kg = piece & 15; const LAS float* s = tile + (kg * 8) * 129 + nl;
;             u32x4 o; o.x = pk2(s[0], s[129]); o.y = pk2(s[258], s[387]); o.z = pk2(s[516], s[645]); o.w = pk2(s[774], s[903]);
;             *(u32x4*)(dst + (size_t)(drow0 + nl) * 2048 + k0 + kg * 8) = o; }
.Lcva_nopf:
	s_lshr_b32 s36, s24, 12
	s_bfe_u32 s30, s24, 0x40008
	s_add_i32 s30, s30, 16
	s_lshl_b32 s30, s30, 24
	s_bfe_u32 s31, s24, 0x40004
	s_and_b32 s32, s24, 15
	v_readlane_b32 s26, v254, 43
	v_readlane_b32 s27, v254, 44
	s_cmp_lg_u32 s36, 0
	s_cselect_b32 s26, s40, s26
	s_cselect_b32 s27, s41, s27
	s_lshl_b32 s33, s31, 20
	s_add_i32 s33, s33, s30
	s_lshl_b32 s37, s32, 9
	s_add_i32 s33, s33, s37
	s_add_u32 s26, s26, s33
	s_addc_u32 s27, s27, 0
	v_readlane_b32 s28, v254, 25
	v_readlane_b32 s29, v254, 26
	s_lshl_b32 s33, s32, 20
	s_add_i32 s33, s33, s30
	s_lshl_b32 s37, s36, 19
	s_add_i32 s33, s33, s37
	s_lshl_b32 s37, s31, 8
	s_add_i32 s33, s33, s37
	s_add_u32 s28, s28, s33
	s_addc_u32 s29, s29, 0
	global_load_dwordx4 v[128:131], v105, s[26:27]
	global_load_dwordx4 v[132:135], v106, s[26:27]
	global_load_dwordx4 v[136:139], v107, s[26:27]
	global_load_dwordx4 v[140:143], v108, s[26:27]
	global_load_dwordx4 v[144:147], v109, s[26:27]
	global_load_dwordx4 v[148:151], v110, s[26:27]
	global_load_dwordx4 v[152:155], v111, s[26:27]
	global_load_dwordx4 v[156:159], v112, s[26:27]
	s_waitcnt vmcnt(7)
	ds_write_b32 v113, v128
	ds_write_b32 v113, v129 offset:4
	ds_write_b32 v113, v130 offset:8
	ds_write_b32 v113, v131 offset:12
	s_waitcnt vmcnt(6)
	ds_write_b32 v113, v132 offset:8256
	ds_write_b32 v113, v133 offset:8260
	ds_write_b32 v113, v134 offset:8264
	ds_write_b32 v113, v135 offset:8268
	s_waitcnt vmcnt(5)
	ds_write_b32 v113, v136 offset:16512
	ds_write_b32 v113, v137 offset:16516
	ds_write_b32 v113, v138 offset:16520
	ds_write_b32 v113, v139 offset:16524
	s_waitcnt vmcnt(4)
	ds_write_b32 v113, v140 offset:24768
	ds_write_b32 v113, v141 offset:24772
	ds_write_b32 v113, v142 offset:24776
	ds_write_b32 v113, v143 offset:24780
	s_waitcnt vmcnt(3)
	ds_write_b32 v113, v144 offset:33024
	ds_write_b32 v113, v145 offset:33028
	ds_write_b32 v113, v146 offset:33032
	ds_write_b32 v113, v147 offset:33036
	s_waitcnt vmcnt(2)
	ds_write_b32 v113, v148 offset:41280
	ds_write_b32 v113, v149 offset:41284
	ds_write_b32 v113, v150 offset:41288
	ds_write_b32 v113, v151 offset:41292
	s_waitcnt vmcnt(1)
	ds_write_b32 v113, v152 offset:49536
	ds_write_b32 v113, v153 offset:49540
	ds_write_b32 v113, v154 offset:49544
	ds_write_b32 v113, v155 offset:49548
	s_waitcnt vmcnt(0)
	ds_write_b32 v113, v156 offset:57792
	ds_write_b32 v113, v157 offset:57796
	ds_write_b32 v113, v158 offset:57800
	ds_write_b32 v113, v159 offset:57804
	s_waitcnt lgkmcnt(0)
	s_barrier
	ds_read_b32 v160, v114
	ds_read_b32 v161, v114 offset:516
	ds_read_b32 v162, v114 offset:1032
	ds_read_b32 v163, v114 offset:1548
	ds_read_b32 v164, v114 offset:2064
	ds_read_b32 v165, v114 offset:2580
	ds_read_b32 v166, v114 offset:3096
	ds_read_b32 v167, v114 offset:3612
	s_waitcnt lgkmcnt(0)
	v_cvt_pk_bf16_f32 v168, v160, v161
	v_cvt_pk_bf16_f32 v169, v162, v163
	v_cvt_pk_bf16_f32 v170, v164, v165
	v_cvt_pk_bf16_f32 v171, v166, v167
	global_store_dwordx4 v115, v[168:171], s[28:29]
	ds_read_b32 v160, v114 offset:128
	ds_read_b32 v161, v114 offset:644
	ds_read_b32 v162, v114 offset:1160
	ds_read_b32 v163, v114 offset:1676
	ds_read_b32 v164, v114 offset:2192
	ds_read_b32 v165, v114 offset:2708
	ds_read_b32 v166, v114 offset:3224
	ds_read_b32 v167, v114 offset:3740
	s_waitcnt lgkmcnt(0)
	v_cvt_pk_bf16_f32 v172, v160, v161
	v_cvt_pk_bf16_f32 v173, v162, v163
	v_cvt_pk_bf16_f32 v174, v164, v165
	v_cvt_pk_bf16_f32 v175, v166, v167
	global_store_dwordx4 v116, v[172:175], s[28:29]
	ds_read_b32 v160, v114 offset:256
	ds_read_b32 v161, v114 offset:772
	ds_read_b32 v162, v114 offset:1288
	ds_read_b32 v163, v114 offset:1804
	ds_read_b32 v164, v114 offset:2320
	ds_read_b32 v165, v114 offset:2836
	ds_read_b32 v166, v114 offset:3352
	ds_read_b32 v167, v114 offset:3868
	s_waitcnt lgkmcnt(0)
	v_cvt_pk_bf16_f32 v168, v160, v161
	v_cvt_pk_bf16_f32 v169, v162, v163
	v_cvt_pk_bf16_f32 v170, v164, v165
	v_cvt_pk_bf16_f32 v171, v166, v167
	global_store_dwordx4 v117, v[168:171], s[28:29]
	ds_read_b32 v160, v114 offset:384
	ds_read_b32 v161, v114 offset:900
	ds_read_b32 v162, v114 offset:1416
	ds_read_b32 v163, v114 offset:1932
	ds_read_b32 v164, v114 offset:2448
	ds_read_b32 v165, v114 offset:2964
	ds_read_b32 v166, v114 offset:3480
	ds_read_b32 v167, v114 offset:3996
	s_waitcnt lgkmcnt(0)
	v_cvt_pk_bf16_f32 v172, v160, v161
	v_cvt_pk_bf16_f32 v173, v162, v163
	v_cvt_pk_bf16_f32 v174, v164, v165
	v_cvt_pk_bf16_f32 v175, v166, v167
	global_store_dwordx4 v118, v[172:175], s[28:29]
	s_cmpk_ge_u32 s25, 0x3c
	s_cbranch_scc1 .Lcva_done
	v_cmp_eq_u32_e32 vcc, 0, v0
	s_and_saveexec_b64 s[34:35], vcc
	s_cbranch_execz .Lcva_t0c
	s_waitcnt vmcnt(0)
	ds_write_b32 v125, v123
	ds_write_b32 v125, v124 offset:4

; #define LAS __attribute__((address_space(3)))
; __device__ __forceinline__ void lds_barrier() { asm volatile("s_waitcnt lgkmcnt(0)" ::: "memory"); __builtin_amdgcn_s_barrier(); asm volatile("" ::: "memory"); }
; __device__ __forceinline__ unsigned xb_add(unsigned* p, unsigned v) { return __hip_atomic_fetch_add(p, v, __ATOMIC_RELAXED, __HIP_MEMORY_SCOPE_AGENT); }
; __device__ __forceinline__ void phase_prologue(const Args& a, LAS unsigned char* lds) {
;     ...
;     unsigned* cq_head = (unsigned*)(a.ws + WS_CTL) + 8192 + 768;
;     volatile LAS int* qs = (volatile LAS int*)(lds + 128 * 129 * 4);
;     int pend = 0, it = 0;
;     if (tid == 0) { qs[0] = (int)xb_add(cq_head, 1u); pend = (int)xb_add(cq_head, 1u); }
;     __syncthreads();
;     for (int u = qs[0]; u < CTOT; u = qs[it & 1]) {
;     ...
;         const int kt = r / NT, ntl = r % NT, k0 = kt * 128, n0 = ntl * 128;
;         const int drow0 = mode == 0 ? n0 : (ntl * 256 + (mode == 2 ? 128 : 0));
;         f32x4 v[8];
; #pragma unroll
;         for (int i = 0; i < 8; ++i) { const int id = tid + 512 * i, row = id >> 5, c4 = id & 31, n = n0 + c4 * 4;
;             v[i] = (f32x4){0.f, 0.f, 0.f, 0.f};
;             if (n < nvalid) v[i] = *(const f32x4*)(src + (size_t)(k0 + row) * ldn + n); }
; #pragma unroll
;         for (int i = 0; i < 8; ++i) { const int id = tid + 512 * i, row = id >> 5, c4 = id & 31;
;             LAS float* tp = tile + row * 129 + c4 * 4; tp[0] = v[i][0]; tp[1] = v[i][1]; tp[2] = v[i][2]; tp[3] = v[i][3]; }
;         lds_barrier();
; #pragma unroll
;         for (int i = 0; i < 4; ++i) { const int piece = tid + 512 * i, nl = piece >> 4, kg = piece & 15; const LAS float* s = tile + (kg * 8) * 129 + nl;
;             u32x4 o; o.x = pk2(s[0], s[129]); o.y = pk2(s[258], s[387]); o.z = pk2(s[516], s[645]); o.w = pk2(s[774], s[903]);
;             *(u32x4*)(dst + (size_t)(drow0 + nl) * 2048 + k0 + kg * 8) = o; }
.Lcvb_f0:
	s_mov_b64 exec, s[34:35]
	s_waitcnt lgkmcnt(0)
	s_barrier
	ds_read_b32 v127, v125 offset:4
	s_waitcnt lgkmcnt(0)
	v_readfirstlane_b32 s25, v127
	s_cmpk_ge_u32 s25, 0xf8
	s_cbranch_scc1 .Lcvb_done
	s_barrier
	v_lshrrev_b32_e32 v104, 5, v0
	v_and_b32_e32 v126, 31, v0
	v_lshlrev_b32_e32 v105, 13, v104
	v_lshl_add_u32 v105, v126, 4, v105
	v_add_u32_e32 v106, 0x20000, v105
	v_add_u32_e32 v107, 0x40000, v105
	v_add_u32_e32 v108, 0x60000, v105
	v_add_u32_e32 v109, 0x80000, v105
	v_add_u32_e32 v110, 0xa0000, v105
	v_add_u32_e32 v111, 0xc0000, v105
	v_add_u32_e32 v112, 0xe0000, v105
	v_mul_u32_u24_e32 v113, 0x204, v104
	v_lshl_add_u32 v113, v126, 4, v113
	v_lshrrev_b32_e32 v127, 4, v0
	v_and_b32_e32 v126, 15, v0
	v_mul_u32_u24_e32 v114, 0x1020, v126
	v_lshl_add_u32 v114, v127, 2, v114
	v_lshlrev_b32_e32 v115, 12, v127
	v_lshl_add_u32 v115, v126, 4, v115
	v_add_u32_e32 v116, 0x20000, v115
	v_add_u32_e32 v117, 0x40000, v115
	v_add_u32_e32 v118, 0x60000, v115
	v_readlane_b32 s42, v254, 27
	v_readlane_b32 s43, v254, 28
	s_sub_u32 s42, s42, 0x28
	s_subb_u32 s43, s43, 0
	s_load_dwordx2 s[40:41], s[42:43], 0x0
	s_waitcnt lgkmcnt(0)
	v_cmp_eq_u32_e32 vcc, 0, v0
	s_and_saveexec_b64 s[34:35], vcc
	s_cbranch_execz .Lcvb_t0a
	global_atomic_add v123, v120, v119, s[94:95] sc0
	s_waitcnt vmcnt(0)
	ds_write_b32 v125, v123
	ds_write_b32 v125, v122 offset:4

; __device__ __forceinline__ void lds_barrier() { asm volatile("s_waitcnt lgkmcnt(0)" ::: "memory"); __builtin_amdgcn_s_barrier(); asm volatile("" ::: "memory"); }
; __device__ __forceinline__ unsigned xb_add(unsigned* p, unsigned v) { return __hip_atomic_fetch_add(p, v, __ATOMIC_RELAXED, __HIP_MEMORY_SCOPE_AGENT); }
; __device__ __forceinline__ void phase_prologue(const Args& a, LAS unsigned char* lds) {
;     ...
;     for (int u = qs[0]; u < CTOT; u = qs[it & 1]) {
;         int r = u; const float* src; int ldn, nvalid, NT, mode = 0; bf16_t* dst;
;     ...
;         ++it;
;         if (tid == 0) { qs[it & 1] = pend; pend = (int)xb_add(cq_head, 1u); }
;         lds_barrier();
.Lcvb_loop:
	ds_read_b32 v126, v125
	ds_read_b32 v127, v125 offset:4
	s_waitcnt lgkmcnt(0)
	v_readfirstlane_b32 s24, v126
	v_readfirstlane_b32 s25, v127
	s_cmpk_gt_u32 s24, 0x1fff
	s_cbranch_scc1 .Lcvb_done
	s_cmpk_ge_u32 s25, 0xf8
	s_cbranch_scc1 .Lcvb_nopf
	v_cmp_eq_u32_e32 vcc, 0, v0
	s_and_saveexec_b64 s[34:35], vcc
	s_cbranch_execz .Lcvb_t0b
	global_atomic_add v123, v120, v119, s[94:95] sc0
	global_atomic_add v124, v121, v122, s[94:95] sc0

; #define LAS __attribute__((address_space(3)))
; __device__ __forceinline__ void lds_barrier() { asm volatile("s_waitcnt lgkmcnt(0)" ::: "memory"); __builtin_amdgcn_s_barrier(); asm volatile("" ::: "memory"); }
; __device__ __forceinline__ void phase_prologue(const Args& a, LAS unsigned char* lds) {
;     ...
;         else { r -= CJ3; const int which = r / CJM; r -= which * CJM; const int mtx = r >> 8; r &= 255; ldn = 2048; nvalid = 2048; NT = 16;
;             if (which == 0) { src = a.in[I_WGATE] + (size_t)mtx * 2048 * 2048; dst = (bf16_t*)(a.ws + WS_WGU) + (size_t)mtx * 4096 * 2048; mode = 1; }
;             else if (which == 1) { src = a.in[I_WUP] + (size_t)mtx * 2048 * 2048; dst = (bf16_t*)(a.ws + WS_WGU) + (size_t)mtx * 4096 * 2048; mode = 2; }
;             else { src = a.in[I_WDOWN] + (size_t)mtx * 2048 * 2048; dst = (bf16_t*)(a.ws + WS_WDN) + (size_t)mtx * 2048 * 2048; } }
;         const int kt = r / NT, ntl = r % NT, k0 = kt * 128, n0 = ntl * 128;
;         const int drow0 = mode == 0 ? n0 : (ntl * 256 + (mode == 2 ? 128 : 0));
;         f32x4 v[8];
; #pragma unroll
;         for (int i = 0; i < 8; ++i) { const int id = tid + 512 * i, row = id >> 5, c4 = id & 31, n = n0 + c4 * 4;
;             v[i] = (f32x4){0.f, 0.f, 0.f, 0.f};
;             if (n < nvalid) v[i] = *(const f32x4*)(src + (size_t)(k0 + row) * ldn + n); }
; #pragma unroll
;         for (int i = 0; i < 8; ++i) { const int id = tid + 512 * i, row = id >> 5, c4 = id & 31;
;             LAS float* tp = tile + row * 129 + c4 * 4; tp[0] = v[i][0]; tp[1] = v[i][1]; tp[2] = v[i][2]; tp[3] = v[i][3]; }
;         lds_barrier();
; #pragma unroll
;         for (int i = 0; i < 4; ++i) { const int piece = tid + 512 * i, nl = piece >> 4, kg = piece & 15; const LAS float* s = tile + (kg * 8) * 129 + nl;
;             u32x4 o; o.x = pk2(s[0], s[129]); o.y = pk2(s[258], s[387]); o.z = pk2(s[516], s[645]); o.w = pk2(s[774], s[903]);
;             *(u32x4*)(dst + (size_t)(drow0 + nl) * 2048 + k0 + kg * 8) = o; }
.Lcvb_nopf:
	s_lshr_b32 s36, s24, 12
	s_bfe_u32 s30, s24, 0x40008
	s_add_i32 s30, s30, 16
	s_lshl_b32 s30, s30, 24
	s_bfe_u32 s31, s24, 0x40004
	s_and_b32 s32, s24, 15
	v_readlane_b32 s26, v254, 43
	v_readlane_b32 s27, v254, 44
	s_cmp_lg_u32 s36, 0
	s_cselect_b32 s26, s40, s26
	s_cselect_b32 s27, s41, s27
	s_lshl_b32 s33, s31, 20
	s_add_i32 s33, s33, s30
	s_lshl_b32 s37, s32, 9
	s_add_i32 s33, s33, s37
	s_add_u32 s26, s26, s33
	s_addc_u32 s27, s27, 0
	v_readlane_b32 s28, v254, 25
	v_readlane_b32 s29, v254, 26
	s_lshl_b32 s33, s32, 20
	s_add_i32 s33, s33, s30
	s_lshl_b32 s37, s36, 19
	s_add_i32 s33, s33, s37
	s_lshl_b32 s37, s31, 8
	s_add_i32 s33, s33, s37
	s_add_u32 s28, s28, s33
	s_addc_u32 s29, s29, 0
	global_load_dwordx4 v[128:131], v105, s[26:27]
	global_load_dwordx4 v[132:135], v106, s[26:27]
	global_load_dwordx4 v[136:139], v107, s[26:27]
	global_load_dwordx4 v[140:143], v108, s[26:27]
	global_load_dwordx4 v[144:147], v109, s[26:27]
	global_load_dwordx4 v[148:151], v110, s[26:27]
	global_load_dwordx4 v[152:155], v111, s[26:27]
	global_load_dwordx4 v[156:159], v112, s[26:27]
	s_waitcnt vmcnt(7)
	ds_write_b32 v113, v128
	ds_write_b32 v113, v129 offset:4
	ds_write_b32 v113, v130 offset:8
	ds_write_b32 v113, v131 offset:12
	s_waitcnt vmcnt(6)
	ds_write_b32 v113, v132 offset:8256
	ds_write_b32 v113, v133 offset:8260
	ds_write_b32 v113, v134 offset:8264
	ds_write_b32 v113, v135 offset:8268
	s_waitcnt vmcnt(5)
	ds_write_b32 v113, v136 offset:16512
	ds_write_b32 v113, v137 offset:16516
	ds_write_b32 v113, v138 offset:16520
	ds_write_b32 v113, v139 offset:16524
	s_waitcnt vmcnt(4)
	ds_write_b32 v113, v140 offset:24768
	ds_write_b32 v113, v141 offset:24772
	ds_write_b32 v113, v142 offset:24776
	ds_write_b32 v113, v143 offset:24780
	s_waitcnt vmcnt(3)
	ds_write_b32 v113, v144 offset:33024
	ds_write_b32 v113, v145 offset:33028
	ds_write_b32 v113, v146 offset:33032
	ds_write_b32 v113, v147 offset:33036
	s_waitcnt vmcnt(2)
	ds_write_b32 v113, v148 offset:41280
	ds_write_b32 v113, v149 offset:41284
	ds_write_b32 v113, v150 offset:41288
	ds_write_b32 v113, v151 offset:41292
	s_waitcnt vmcnt(1)
	ds_write_b32 v113, v152 offset:49536
	ds_write_b32 v113, v153 offset:49540
	ds_write_b32 v113, v154 offset:49544
	ds_write_b32 v113, v155 offset:49548
	s_waitcnt vmcnt(0)
	ds_write_b32 v113, v156 offset:57792
	ds_write_b32 v113, v157 offset:57796
	ds_write_b32 v113, v158 offset:57800
	ds_write_b32 v113, v159 offset:57804
	s_waitcnt lgkmcnt(0)
	s_barrier
	ds_read_b32 v160, v114
	ds_read_b32 v161, v114 offset:516
	ds_read_b32 v162, v114 offset:1032
	ds_read_b32 v163, v114 offset:1548
	ds_read_b32 v164, v114 offset:2064
	ds_read_b32 v165, v114 offset:2580
	ds_read_b32 v166, v114 offset:3096
	ds_read_b32 v167, v114 offset:3612
	s_waitcnt lgkmcnt(0)
	v_cvt_pk_bf16_f32 v168, v160, v161
	v_cvt_pk_bf16_f32 v169, v162, v163
	v_cvt_pk_bf16_f32 v170, v164, v165
	v_cvt_pk_bf16_f32 v171, v166, v167
	global_store_dwordx4 v115, v[168:171], s[28:29]
	ds_read_b32 v160, v114 offset:128
	ds_read_b32 v161, v114 offset:644
	ds_read_b32 v162, v114 offset:1160
	ds_read_b32 v163, v114 offset:1676
	ds_read_b32 v164, v114 offset:2192
	ds_read_b32 v165, v114 offset:2708
	ds_read_b32 v166, v114 offset:3224
	ds_read_b32 v167, v114 offset:3740
	s_waitcnt lgkmcnt(0)
	v_cvt_pk_bf16_f32 v172, v160, v161
	v_cvt_pk_bf16_f32 v173, v162, v163
	v_cvt_pk_bf16_f32 v174, v164, v165
	v_cvt_pk_bf16_f32 v175, v166, v167
	global_store_dwordx4 v116, v[172:175], s[28:29]
	ds_read_b32 v160, v114 offset:256
	ds_read_b32 v161, v114 offset:772
	ds_read_b32 v162, v114 offset:1288
	ds_read_b32 v163, v114 offset:1804
	ds_read_b32 v164, v114 offset:2320
	ds_read_b32 v165, v114 offset:2836
	ds_read_b32 v166, v114 offset:3352
	ds_read_b32 v167, v114 offset:3868
	s_waitcnt lgkmcnt(0)
	v_cvt_pk_bf16_f32 v168, v160, v161
	v_cvt_pk_bf16_f32 v169, v162, v163
	v_cvt_pk_bf16_f32 v170, v164, v165
	v_cvt_pk_bf16_f32 v171, v166, v167
	global_store_dwordx4 v117, v[168:171], s[28:29]
	ds_read_b32 v160, v114 offset:384
	ds_read_b32 v161, v114 offset:900
	ds_read_b32 v162, v114 offset:1416
	ds_read_b32 v163, v114 offset:1932
	ds_read_b32 v164, v114 offset:2448
	ds_read_b32 v165, v114 offset:2964
	ds_read_b32 v166, v114 offset:3480
	ds_read_b32 v167, v114 offset:3996
	s_waitcnt lgkmcnt(0)
	v_cvt_pk_bf16_f32 v172, v160, v161
	v_cvt_pk_bf16_f32 v173, v162, v163
	v_cvt_pk_bf16_f32 v174, v164, v165
	v_cvt_pk_bf16_f32 v175, v166, v167
	global_store_dwordx4 v118, v[172:175], s[28:29]
	s_cmpk_ge_u32 s25, 0xf8
	s_cbranch_scc1 .Lcvb_done
	v_cmp_eq_u32_e32 vcc, 0, v0
	s_and_saveexec_b64 s[34:35], vcc
	s_cbranch_execz .Lcvb_t0c
	s_waitcnt vmcnt(0)
	ds_write_b32 v125, v123
	ds_write_b32 v125, v124 offset:4
